# instruction selection: merged two constant multiplies in the clamped-SwiGLU epilogue; one static s_setprio raise for waves 4-7 in the attention unit
# speedup vs baseline: 1.0019x; 1.0019x over previous
.LBB0_912:
	s_setprio 0
	s_or_b64 exec, exec, s[2:3]
	s_waitcnt lgkmcnt(0)
	ds_read_b128 v[34:37], v67 offset:49280
	ds_read_b128 v[38:41], v67 offset:49312
	s_lshl_b64 s[0:1], s[4:5], 11
	s_add_u32 s0, s40, s0
	s_addc_u32 s1, s39, s1
	s_waitcnt lgkmcnt(1)
	v_rcp_f32_e32 v42, v34
	s_lshl_b32 s2, s34, 12
	s_add_i32 s2, s2, 0
	v_lshlrev_b32_e32 v1, 1, v1
	v_lshlrev_b32_e32 v50, 9, v193
	v_mul_f32_e32 v18, v18, v42
	v_rcp_f32_e32 v43, v35
	v_add3_u32 v1, s2, v1, v50
	v_bfe_u32 v50, v18, 16, 1
	v_add3_u32 v18, v18, v50, s33
	v_mul_f32_e32 v2, v2, v42
	ds_write_b16_d16_hi v1, v18 offset:51200
	v_bfe_u32 v18, v2, 16, 1
	v_add3_u32 v2, v2, v18, s33
	ds_write_b16_d16_hi v1, v2 offset:51264
	v_mul_f32_e32 v2, v19, v43
	v_bfe_u32 v18, v2, 16, 1
	v_rcp_f32_e32 v44, v36
	v_add3_u32 v2, v2, v18, s33
	ds_write_b16_d16_hi v1, v2 offset:51328
	v_mul_f32_e32 v2, v3, v43
	v_bfe_u32 v3, v2, 16, 1
	v_add3_u32 v2, v2, v3, s33
	ds_write_b16_d16_hi v1, v2 offset:51392
	v_mul_f32_e32 v2, v20, v44
	v_bfe_u32 v3, v2, 16, 1
	v_rcp_f32_e32 v45, v37
	v_add3_u32 v2, v2, v3, s33
	ds_write_b16_d16_hi v1, v2 offset:51456
	v_mul_f32_e32 v2, v4, v44
	v_bfe_u32 v3, v2, 16, 1
	v_add3_u32 v2, v2, v3, s33
	ds_write_b16_d16_hi v1, v2 offset:51520
	v_mul_f32_e32 v2, v21, v45
	v_bfe_u32 v3, v2, 16, 1
	s_waitcnt lgkmcnt(6)
	v_rcp_f32_e32 v46, v38
	v_add3_u32 v2, v2, v3, s33
	ds_write_b16_d16_hi v1, v2 offset:51584
	v_mul_f32_e32 v2, v5, v45
	v_bfe_u32 v3, v2, 16, 1
	v_add3_u32 v2, v2, v3, s33
	ds_write_b16_d16_hi v1, v2 offset:51648
	v_mul_f32_e32 v2, v22, v46
	v_bfe_u32 v3, v2, 16, 1
	v_rcp_f32_e32 v47, v39
	v_add3_u32 v2, v2, v3, s33
	ds_write_b16_d16_hi v1, v2 offset:52224
	v_mul_f32_e32 v2, v6, v46
	v_bfe_u32 v3, v2, 16, 1
	v_add3_u32 v2, v2, v3, s33
	ds_write_b16_d16_hi v1, v2 offset:52288
	v_mul_f32_e32 v2, v23, v47
	v_bfe_u32 v3, v2, 16, 1
	v_rcp_f32_e32 v48, v40
	v_add3_u32 v2, v2, v3, s33
	ds_write_b16_d16_hi v1, v2 offset:52352
	v_mul_f32_e32 v2, v7, v47
	v_bfe_u32 v3, v2, 16, 1
	v_add3_u32 v2, v2, v3, s33
	ds_write_b16_d16_hi v1, v2 offset:52416
	v_mul_f32_e32 v2, v24, v48
	v_bfe_u32 v3, v2, 16, 1
	v_rcp_f32_e32 v49, v41
	v_add3_u32 v2, v2, v3, s33
	ds_read_b128 v[34:37], v67 offset:49344
	ds_read_b128 v[38:41], v67 offset:49376
	ds_write_b16_d16_hi v1, v2 offset:52480
	v_mul_f32_e32 v2, v8, v48
	v_bfe_u32 v3, v2, 16, 1
	v_add3_u32 v2, v2, v3, s33
	ds_write_b16_d16_hi v1, v2 offset:52544
	v_mul_f32_e32 v2, v25, v49
	v_bfe_u32 v3, v2, 16, 1
	s_waitcnt lgkmcnt(3)
	v_rcp_f32_e32 v34, v34
	v_add3_u32 v2, v2, v3, s33
	ds_write_b16_d16_hi v1, v2 offset:52608
	v_mul_f32_e32 v2, v9, v49
	v_bfe_u32 v3, v2, 16, 1
	v_add3_u32 v2, v2, v3, s33
	ds_write_b16_d16_hi v1, v2 offset:52672
	v_mul_f32_e32 v2, v26, v34
	v_bfe_u32 v3, v2, 16, 1
	v_rcp_f32_e32 v35, v35
	v_add3_u32 v2, v2, v3, s33
	ds_write_b16_d16_hi v1, v2 offset:53248
	v_mul_f32_e32 v2, v10, v34
	v_bfe_u32 v3, v2, 16, 1
	v_add3_u32 v2, v2, v3, s33
	ds_write_b16_d16_hi v1, v2 offset:53312
	v_mul_f32_e32 v2, v27, v35
	v_bfe_u32 v3, v2, 16, 1
	v_rcp_f32_e32 v36, v36
	v_add3_u32 v2, v2, v3, s33
	ds_write_b16_d16_hi v1, v2 offset:53376
	v_mul_f32_e32 v2, v11, v35
	v_bfe_u32 v3, v2, 16, 1
	v_add3_u32 v2, v2, v3, s33
	ds_write_b16_d16_hi v1, v2 offset:53440
	v_mul_f32_e32 v2, v28, v36
	v_bfe_u32 v3, v2, 16, 1
	v_rcp_f32_e32 v37, v37
	v_add3_u32 v2, v2, v3, s33
	ds_write_b16_d16_hi v1, v2 offset:53504
	v_mul_f32_e32 v2, v12, v36
	v_bfe_u32 v3, v2, 16, 1
	v_add3_u32 v2, v2, v3, s33
	ds_write_b16_d16_hi v1, v2 offset:53568
	v_mul_f32_e32 v2, v29, v37
	v_bfe_u32 v3, v2, 16, 1
	s_waitcnt lgkmcnt(10)
	v_rcp_f32_e32 v38, v38
	v_add3_u32 v2, v2, v3, s33
	ds_write_b16_d16_hi v1, v2 offset:53632
	v_mul_f32_e32 v2, v13, v37
	v_bfe_u32 v3, v2, 16, 1
	v_add3_u32 v2, v2, v3, s33
	ds_write_b16_d16_hi v1, v2 offset:53696
	v_mul_f32_e32 v2, v30, v38
	v_bfe_u32 v3, v2, 16, 1
	v_rcp_f32_e32 v39, v39
	v_add3_u32 v2, v2, v3, s33
	ds_write_b16_d16_hi v1, v2 offset:54272
	v_mul_f32_e32 v2, v14, v38
	v_bfe_u32 v3, v2, 16, 1
	v_add3_u32 v2, v2, v3, s33
	ds_write_b16_d16_hi v1, v2 offset:54336
	v_mul_f32_e32 v2, v31, v39
	v_bfe_u32 v3, v2, 16, 1
	v_rcp_f32_e32 v40, v40
	v_add3_u32 v2, v2, v3, s33
	ds_write_b16_d16_hi v1, v2 offset:54400
	v_mul_f32_e32 v2, v15, v39
	v_bfe_u32 v3, v2, 16, 1
	v_add3_u32 v2, v2, v3, s33
	ds_write_b16_d16_hi v1, v2 offset:54464
	v_mul_f32_e32 v2, v32, v40
	v_bfe_u32 v3, v2, 16, 1
	v_rcp_f32_e32 v41, v41
	v_add3_u32 v2, v2, v3, s33
	ds_write_b16_d16_hi v1, v2 offset:54528
	v_mul_f32_e32 v2, v16, v40
	v_bfe_u32 v3, v2, 16, 1
	v_add3_u32 v2, v2, v3, s33
	ds_write_b16_d16_hi v1, v2 offset:54592
	v_mul_f32_e32 v2, v33, v41
	v_bfe_u32 v3, v2, 16, 1
	v_add3_u32 v2, v2, v3, s33
	ds_write_b16_d16_hi v1, v2 offset:54656
	v_mul_f32_e32 v2, v17, v41
	v_bfe_u32 v3, v2, 16, 1
	v_add3_u32 v2, v2, v3, s33
	ds_write_b16_d16_hi v1, v2 offset:54720
	s_add_u32 s0, s0, s28
	v_lshlrev_b32_e32 v2, 1, v183
	s_addc_u32 s1, s1, 0
	v_and_b32_e32 v100, 0x70, v2
	v_lshrrev_b32_e32 v1, 3, v182
	v_add_u32_e32 v14, s2, v100
	v_lshl_add_u64 v[2:3], s[0:1], 0, v[100:101]
	s_mov_b64 s[0:1], 0x49000400
	s_waitcnt lgkmcnt(0)
	v_lshl_add_u64 v[10:11], v[2:3], 0, s[0:1]
	v_lshl_add_u32 v2, v1, 7, v14
	v_or_b32_e32 v15, 8, v1
	ds_read_b128 v[2:5], v2 offset:51200
	v_lshl_add_u32 v6, v15, 7, v14
	ds_read_b128 v[6:9], v6 offset:51200
	v_lshlrev_b32_e32 v100, 11, v1
	v_lshl_add_u64 v[12:13], v[10:11], 0, v[100:101]
	v_lshlrev_b32_e32 v100, 11, v15
	s_waitcnt lgkmcnt(1)
	global_store_dwordx4 v[12:13], v[2:5], off
	s_nop 1
	v_lshl_add_u64 v[2:3], v[10:11], 0, v[100:101]
	s_waitcnt lgkmcnt(0)
	global_store_dwordx4 v[2:3], v[6:9], off
	s_nop 1
	v_or_b32_e32 v6, 16, v1
	v_lshl_add_u32 v2, v6, 7, v14
	v_or_b32_e32 v1, 24, v1
	ds_read_b128 v[2:5], v2 offset:51200
	v_lshlrev_b32_e32 v100, 11, v6
	v_lshl_add_u32 v6, v1, 7, v14
	ds_read_b128 v[6:9], v6 offset:51200
	v_lshl_add_u64 v[12:13], v[10:11], 0, v[100:101]
	v_lshlrev_b32_e32 v100, 11, v1
	s_waitcnt lgkmcnt(1)
	global_store_dwordx4 v[12:13], v[2:5], off
	s_nop 1
	v_lshl_add_u64 v[2:3], v[10:11], 0, v[100:101]
	s_waitcnt lgkmcnt(0)
	global_store_dwordx4 v[2:3], v[6:9], off
	s_waitcnt lgkmcnt(0)
	s_barrier

.LBB0_992:
	s_or_b64 exec, exec, s[0:1]
	s_waitcnt vmcnt(0)
	v_sub_f32_e32 v1, v1, v14
	s_mov_b32 s0, 0xc3160000
	s_ashr_i32 s34, s3, 6
	s_cmp_lt_i32 s34, 4
	s_cbranch_scc1 .Lattn_prio_skip
	s_setprio 1
.Lattn_prio_skip:
	s_lshl_b32 s50, s2, 12
	v_cmp_le_f32_e32 vcc, s0, v1
	s_ff1_i32_b64 s0, vcc
	s_cmp_lg_u64 vcc, 0
	s_cselect_b32 s47, s0, 0
	s_and_b32 s46, s47, -2
	s_lshl_b32 s0, s46, 6
	s_sub_i32 s41, s45, s46
	s_ashr_i32 s1, s0, 31
	s_add_u32 s2, s50, s0
	s_addc_u32 s3, 0, s1
	s_lshl_b64 s[2:3], s[2:3], 10
	s_lshl_b32 s4, s49, 7
	s_add_u32 s2, s40, s2
	s_addc_u32 s3, s39, s3
	s_add_u32 s2, s2, s4
	s_addc_u32 s3, s3, 0
	v_lshlrev_b32_e32 v100, 10, v182
	s_lshl_b32 s4, s34, 3
	v_lshl_add_u64 v[2:3], s[2:3], 0, v[100:101]
	s_ashr_i32 s5, s4, 31
	v_lshl_add_u64 v[2:3], s[4:5], 1, v[2:3]
	s_lshl_b32 s5, s34, 4
	v_lshrrev_b32_e32 v1, 2, v182
	v_and_or_b32 v1, s5, 48, v1
	v_lshlrev_b32_e32 v100, 10, v1
	v_lshl_add_u64 v[4:5], s[2:3], 0, v[100:101]
	s_and_b32 s2, s4, 0xffffffe0
	v_lshlrev_b32_e32 v183, 3, v0
	s_ashr_i32 s3, s2, 31
	v_and_b32_e32 v192, 24, v183
	v_lshl_add_u64 v[4:5], s[2:3], 1, v[4:5]
	v_lshlrev_b32_e32 v100, 1, v192
	s_mov_b64 s[6:7], 0x3f000000
	v_lshl_add_u64 v[4:5], v[4:5], 0, v[100:101]
	s_mov_b64 s[2:3], 0x40000000
	s_lshl_b32 s42, s34, 10
	v_lshl_add_u64 v[184:185], v[2:3], 0, s[6:7]
	v_lshl_add_u64 v[186:187], v[4:5], 0, s[2:3]
	s_add_i32 s42, s42, 0
	s_mov_b32 s2, m0
	s_mov_b32 m0, s42
	s_nop 0
	global_load_lds_dwordx4 v[184:185], off
	s_mov_b32 m0, s2
	s_add_i32 s43, s42, 0x6000
	s_mov_b32 s2, m0
	s_mov_b32 m0, s43
	s_nop 0
	global_load_lds_dwordx4 v[186:187], off
	s_mov_b32 m0, s2
	s_mov_b64 s[2:3], 0x3f010000
	v_lshl_add_u64 v[2:3], v[2:3], 0, s[2:3]
	s_add_i32 s2, s42, 0x2000
	s_mov_b32 s3, m0
	s_mov_b32 m0, s2
	s_nop 0
	global_load_lds_dwordx4 v[2:3], off
	s_mov_b32 m0, s3
	s_lshl_b32 s48, s41, 6
	s_lshl_b64 s[0:1], s[0:1], 2
	s_add_u32 s28, s26, s0
	s_addc_u32 s29, s27, s1
	v_cmp_gt_i32_e64 s[12:13], s48, v0
	v_mov_b32_e32 v16, 0
	v_ashrrev_i32_e32 v1, 31, v0
	v_mov_b32_e32 v17, 0
	s_and_saveexec_b64 s[0:1], s[12:13]
	s_cbranch_execz .LBB0_994
	v_lshl_add_u64 v[2:3], v[0:1], 2, s[28:29]
	global_load_dword v17, v[2:3], off

.LBB0_1525:
	s_add_i32 s30, s29, s45
	s_ashr_i32 s31, s30, 31
	s_lshl_b64 s[30:31], s[30:31], 13
	v_lshl_or_b32 v146, s8, 7, v236
	s_add_u32 s30, s42, s30
	s_addc_u32 s31, s16, s31
	v_ashrrev_i32_e32 v147, 31, v146
	v_lshl_add_u64 v[44:45], v[146:147], 2, s[30:31]
	global_load_dwordx4 v[40:43], v[44:45], off offset:16
	global_load_dwordx4 v[56:59], v[44:45], off
	s_mov_b64 s[30:31], 0x1000
	s_movk_i32 s9, 0x1000
	v_lshl_add_u64 v[46:47], v[44:45], 0, s[30:31]
	v_add_co_u32_e32 v44, vcc, s9, v44
	s_ashr_i32 s29, s28, 31
	s_nop 0
	v_addc_co_u32_e32 v45, vcc, 0, v45, vcc
	global_load_dwordx4 v[60:63], v[44:45], off
	s_nop 0
	global_load_dwordx4 v[44:47], v[46:47], off offset:16
	s_lshl_b64 s[28:29], s[28:29], 19
	s_mov_b32 s9, 0x8000
	s_waitcnt vmcnt(0)
	v_add_f32_e32 v134, v134, v40
	v_add_f32_e32 v142, v142, v56
	v_min_f32_e32 v142, 0x40e00000, v142
	v_mul_f32_e32 v148, 0xc01d265f, v142
	v_exp_f32_e32 v148, v148
	v_min_f32_e32 v134, 0x40e00000, v134
	v_add_f32_e32 v126, v126, v56
	v_min_f32_e32 v126, 0x40e00000, v126
	v_add_f32_e32 v148, 1.0, v148
	v_rcp_f32_e32 v148, v148
	v_add_f32_e32 v138, v138, v60
	v_med3_f32 v138, v138, s63, v230
	v_add_f32_e32 v138, 1.0, v138
	v_mul_f32_e32 v142, v142, v148
	v_mul_f32_e32 v138, v138, v142
	v_add_f32_e32 v142, v143, v57
	v_min_f32_e32 v142, 0x40e00000, v142
	v_mul_f32_e32 v143, 0xc01d265f, v142
	v_exp_f32_e32 v143, v143
	v_add_f32_e32 v139, v139, v61
	v_med3_f32 v139, v139, s63, v230
	v_add_f32_e32 v139, 1.0, v139
	v_add_f32_e32 v143, 1.0, v143
	v_rcp_f32_e32 v143, v143
	v_add_f32_e32 v140, v140, v62
	v_med3_f32 v140, v140, s63, v230
	v_add_f32_e32 v140, 1.0, v140
	v_mul_f32_e32 v142, v142, v143
	v_mul_f32_e32 v139, v139, v142
	v_add_f32_e32 v142, v144, v58
	v_min_f32_e32 v142, 0x40e00000, v142
	v_mul_f32_e32 v143, 0xc01d265f, v142
	v_exp_f32_e32 v143, v143
	v_add_f32_e32 v141, v141, v63
	v_med3_f32 v141, v141, s63, v230
	v_add_f32_e32 v141, 1.0, v141
	v_add_f32_e32 v143, 1.0, v143
	v_rcp_f32_e32 v143, v143
	v_add_f32_e32 v130, v130, v44
	v_med3_f32 v130, v130, s63, v230
	v_add_f32_e32 v130, 1.0, v130
	v_mul_f32_e32 v142, v142, v143
	v_mul_f32_e32 v140, v140, v142
	v_add_f32_e32 v142, v145, v59
	v_min_f32_e32 v142, 0x40e00000, v142
	v_mul_f32_e32 v143, 0xc01d265f, v142
	v_exp_f32_e32 v143, v143
	v_add_f32_e32 v131, v131, v45
	v_med3_f32 v131, v131, s63, v230
	v_add_f32_e32 v131, 1.0, v131
	v_add_f32_e32 v143, 1.0, v143
	v_rcp_f32_e32 v143, v143
	v_add_f32_e32 v132, v132, v46
	v_med3_f32 v132, v132, s63, v230
	v_add_f32_e32 v132, 1.0, v132
	v_mul_f32_e32 v142, v142, v143
	v_mul_f32_e32 v141, v141, v142
	v_mul_f32_e32 v142, 0xc01d265f, v134
	v_exp_f32_e32 v142, v142
	v_add_f32_e32 v133, v133, v47
	v_med3_f32 v133, v133, s63, v230
	v_add_f32_e32 v133, 1.0, v133
	v_add_f32_e32 v142, 1.0, v142
	v_rcp_f32_e32 v142, v142
	v_add_f32_e32 v122, v122, v60
	v_med3_f32 v122, v122, s63, v230
	v_add_f32_e32 v122, 1.0, v122
	v_mul_f32_e32 v134, v134, v142
	v_mul_f32_e32 v130, v130, v134
	v_add_f32_e32 v134, v135, v41
	v_min_f32_e32 v134, 0x40e00000, v134
	v_mul_f32_e32 v135, 0xc01d265f, v134
	v_exp_f32_e32 v135, v135
	v_add_f32_e32 v123, v123, v61
	v_med3_f32 v123, v123, s63, v230
	v_add_f32_e32 v123, 1.0, v123
	v_add_f32_e32 v135, 1.0, v135
	v_rcp_f32_e32 v135, v135
	v_add_f32_e32 v124, v124, v62
	v_med3_f32 v124, v124, s63, v230
	v_add_f32_e32 v124, 1.0, v124
	v_mul_f32_e32 v134, v134, v135
	v_mul_f32_e32 v131, v131, v134
	v_add_f32_e32 v134, v136, v42
	v_min_f32_e32 v134, 0x40e00000, v134
	v_mul_f32_e32 v135, 0xc01d265f, v134
	v_exp_f32_e32 v135, v135
	v_add_f32_e32 v125, v125, v63
	v_med3_f32 v125, v125, s63, v230
	v_add_f32_e32 v118, v118, v40
	v_add_f32_e32 v135, 1.0, v135
	v_rcp_f32_e32 v135, v135
	v_add_f32_e32 v125, 1.0, v125
	v_min_f32_e32 v118, 0x40e00000, v118
	v_add_f32_e32 v114, v114, v44
	v_mul_f32_e32 v134, v134, v135
	v_mul_f32_e32 v135, v132, v134
	v_add_f32_e32 v132, v137, v43
	v_min_f32_e32 v132, 0x40e00000, v132
	v_mul_f32_e32 v134, 0xc01d265f, v132
	v_exp_f32_e32 v134, v134
	v_med3_f32 v114, v114, s63, v230
	v_add_f32_e32 v114, 1.0, v114
	v_add_f32_e32 v115, v115, v45
	v_add_f32_e32 v134, 1.0, v134
	v_rcp_f32_e32 v134, v134
	v_med3_f32 v115, v115, s63, v230
	v_add_f32_e32 v115, 1.0, v115
	v_add_f32_e32 v110, v110, v56
	v_mul_f32_e32 v132, v132, v134
	v_mul_f32_e32 v136, v133, v132
	v_cvt_pk_bf16_f32 v132, v138, v139
	v_cvt_pk_bf16_f32 v133, v140, v141
	v_cvt_pk_bf16_f32 v134, v130, v131
	v_lshl_add_u64 v[130:131], v[206:207], 0, s[28:29]
	v_lshl_add_u64 v[130:131], v[146:147], 1, v[130:131]
	v_cvt_pk_bf16_f32 v135, v135, v136
	global_store_dwordx4 v[130:131], v[132:135], off
	v_min_f32_e32 v110, 0x40e00000, v110
	v_add_f32_e32 v106, v106, v60
	v_mul_f32_e32 v132, 0xc01d265f, v126
	v_exp_f32_e32 v132, v132
	v_med3_f32 v106, v106, s63, v230
	v_add_f32_e32 v106, 1.0, v106
	v_add_f32_e32 v107, v107, v61
	v_add_f32_e32 v132, 1.0, v132
	v_rcp_f32_e32 v132, v132
	v_med3_f32 v107, v107, s63, v230
	v_add_f32_e32 v107, 1.0, v107
	v_add_f32_e32 v108, v108, v62
	v_mul_f32_e32 v126, v126, v132
	v_mul_f32_e32 v122, v122, v126
	v_add_f32_e32 v126, v127, v57
	v_min_f32_e32 v126, 0x40e00000, v126
	v_mul_f32_e32 v127, 0xc01d265f, v126
	v_exp_f32_e32 v127, v127
	v_med3_f32 v108, v108, s63, v230
	v_add_f32_e32 v108, 1.0, v108
	v_add_f32_e32 v109, v109, v63
	v_add_f32_e32 v127, 1.0, v127
	v_rcp_f32_e32 v127, v127
	v_med3_f32 v109, v109, s63, v230
	v_add_f32_e32 v102, v102, v40
	v_add_f32_e32 v109, 1.0, v109
	v_mul_f32_e32 v126, v126, v127
	v_mul_f32_e32 v123, v123, v126
	v_add_f32_e32 v126, v128, v58
	v_min_f32_e32 v126, 0x40e00000, v126
	v_mul_f32_e32 v127, 0xc01d265f, v126
	v_exp_f32_e32 v127, v127
	v_min_f32_e32 v102, 0x40e00000, v102
	v_add_f32_e32 v96, v96, v44
	v_med3_f32 v96, v96, s63, v230
	v_add_f32_e32 v127, 1.0, v127
	v_rcp_f32_e32 v127, v127
	v_add_f32_e32 v96, 1.0, v96
	v_add_f32_e32 v97, v97, v45
	v_med3_f32 v97, v97, s63, v230
	v_mul_f32_e32 v126, v126, v127
	v_mul_f32_e32 v124, v124, v126
	v_add_f32_e32 v126, v129, v59
	v_min_f32_e32 v126, 0x40e00000, v126
	v_mul_f32_e32 v127, 0xc01d265f, v126
	v_exp_f32_e32 v127, v127
	v_add_f32_e32 v97, 1.0, v97
	v_add_f32_e32 v92, v92, v56
	v_min_f32_e32 v92, 0x40e00000, v92
	v_add_f32_e32 v127, 1.0, v127
	v_rcp_f32_e32 v127, v127
	v_add_f32_e32 v88, v88, v60
	v_med3_f32 v88, v88, s63, v230
	v_add_f32_e32 v88, 1.0, v88
	v_mul_f32_e32 v126, v126, v127
	v_mul_f32_e32 v125, v125, v126
	v_mul_f32_e32 v126, 0xc01d265f, v118
	v_exp_f32_e32 v126, v126
	v_add_f32_e32 v89, v89, v61
	v_med3_f32 v89, v89, s63, v230
	v_add_f32_e32 v89, 1.0, v89
	v_add_f32_e32 v126, 1.0, v126
	v_rcp_f32_e32 v126, v126
	v_add_f32_e32 v90, v90, v62
	v_med3_f32 v90, v90, s63, v230
	v_add_f32_e32 v90, 1.0, v90
	v_mul_f32_e32 v118, v118, v126
	v_mul_f32_e32 v118, v114, v118
	v_add_f32_e32 v114, v119, v41
	v_min_f32_e32 v114, 0x40e00000, v114
	v_mul_f32_e32 v119, 0xc01d265f, v114
	v_exp_f32_e32 v119, v119
	v_add_f32_e32 v91, v91, v63
	v_med3_f32 v91, v91, s63, v230
	v_add_f32_e32 v84, v84, v40
	v_add_f32_e32 v119, 1.0, v119
	v_rcp_f32_e32 v119, v119
	v_add_f32_e32 v91, 1.0, v91
	v_min_f32_e32 v84, 0x40e00000, v84
	v_add_f32_e32 v80, v80, v44
	v_mul_f32_e32 v114, v114, v119
	v_mul_f32_e32 v119, v115, v114
	v_add_f32_e32 v114, v120, v42
	v_min_f32_e32 v114, 0x40e00000, v114
	v_add_f32_e32 v115, v116, v46
	v_mul_f32_e32 v116, 0xc01d265f, v114
	v_exp_f32_e32 v116, v116
	v_med3_f32 v115, v115, s63, v230
	v_add_f32_e32 v115, 1.0, v115
	v_med3_f32 v80, v80, s63, v230
	v_add_f32_e32 v116, 1.0, v116
	v_rcp_f32_e32 v116, v116
	v_add_f32_e32 v80, 1.0, v80
	v_add_f32_e32 v81, v81, v45
	v_med3_f32 v81, v81, s63, v230
	v_mul_f32_e32 v114, v114, v116
	v_mul_f32_e32 v120, v115, v114
	v_add_f32_e32 v114, v121, v43
	v_min_f32_e32 v114, 0x40e00000, v114
	v_mul_f32_e32 v116, 0xc01d265f, v114
	v_exp_f32_e32 v116, v116
	v_add_f32_e32 v115, v117, v47
	v_med3_f32 v115, v115, s63, v230
	v_add_f32_e32 v115, 1.0, v115
	v_add_f32_e32 v116, 1.0, v116
	v_rcp_f32_e32 v116, v116
	v_add_f32_e32 v81, 1.0, v81
	v_add_f32_e32 v76, v76, v56
	v_min_f32_e32 v76, 0x40e00000, v76
	v_mul_f32_e32 v114, v114, v116
	v_mul_f32_e32 v117, v115, v114
	v_cvt_pk_bf16_f32 v114, v122, v123
	v_cvt_pk_bf16_f32 v115, v124, v125
	v_cvt_pk_bf16_f32 v116, v118, v119
	v_add_co_u32_e32 v118, vcc, s9, v130
	v_cvt_pk_bf16_f32 v117, v120, v117
	s_mov_b32 s9, 0x10000
	s_nop 0
	v_addc_co_u32_e32 v119, vcc, 0, v131, vcc
	global_store_dwordx4 v[118:119], v[114:117], off
	v_add_f32_e32 v72, v72, v60
	v_med3_f32 v72, v72, s63, v230
	v_mul_f32_e32 v114, 0xc01d265f, v110
	v_exp_f32_e32 v114, v114
	v_add_f32_e32 v72, 1.0, v72
	v_add_f32_e32 v73, v73, v61
	v_med3_f32 v73, v73, s63, v230
	v_add_f32_e32 v114, 1.0, v114
	v_rcp_f32_e32 v114, v114
	v_add_f32_e32 v73, 1.0, v73
	v_add_f32_e32 v74, v74, v62
	v_med3_f32 v74, v74, s63, v230
	v_mul_f32_e32 v110, v110, v114
	v_mul_f32_e32 v106, v106, v110
	v_add_f32_e32 v110, v111, v57
	v_min_f32_e32 v110, 0x40e00000, v110
	v_mul_f32_e32 v111, 0xc01d265f, v110
	v_exp_f32_e32 v111, v111
	v_add_f32_e32 v74, 1.0, v74
	v_add_f32_e32 v75, v75, v63
	v_med3_f32 v75, v75, s63, v230
	v_add_f32_e32 v111, 1.0, v111
	v_rcp_f32_e32 v111, v111
	v_add_f32_e32 v68, v68, v40
	v_add_f32_e32 v75, 1.0, v75
	v_min_f32_e32 v68, 0x40e00000, v68
	v_mul_f32_e32 v110, v110, v111
	v_mul_f32_e32 v107, v107, v110
	v_add_f32_e32 v110, v112, v58
	v_min_f32_e32 v110, 0x40e00000, v110
	v_mul_f32_e32 v111, 0xc01d265f, v110
	v_exp_f32_e32 v111, v111
	v_add_f32_e32 v64, v64, v44
	v_med3_f32 v64, v64, s63, v230
	v_add_f32_e32 v64, 1.0, v64
	v_add_f32_e32 v111, 1.0, v111
	v_rcp_f32_e32 v111, v111
	v_add_f32_e32 v65, v65, v45
	v_med3_f32 v65, v65, s63, v230
	v_add_f32_e32 v65, 1.0, v65
	v_mul_f32_e32 v110, v110, v111
	v_mul_f32_e32 v108, v108, v110
	v_add_f32_e32 v110, v113, v59
	v_min_f32_e32 v110, 0x40e00000, v110
	v_mul_f32_e32 v111, 0xc01d265f, v110
	v_exp_f32_e32 v111, v111
	v_add_f32_e32 v52, v52, v56
	v_min_f32_e32 v52, 0x40e00000, v52
	v_add_f32_e32 v48, v48, v60
	v_add_f32_e32 v111, 1.0, v111
	v_rcp_f32_e32 v111, v111
	v_med3_f32 v48, v48, s63, v230
	v_add_f32_e32 v48, 1.0, v48
	v_add_f32_e32 v49, v49, v61
	v_mul_f32_e32 v110, v110, v111
	v_mul_f32_e32 v109, v109, v110
	v_mul_f32_e32 v110, 0xc01d265f, v102
	v_exp_f32_e32 v110, v110
	v_med3_f32 v49, v49, s63, v230
	v_add_f32_e32 v49, 1.0, v49
	v_add_f32_e32 v50, v50, v62
	v_add_f32_e32 v110, 1.0, v110
	v_rcp_f32_e32 v110, v110
	v_med3_f32 v50, v50, s63, v230
	v_add_f32_e32 v50, 1.0, v50
	v_add_f32_e32 v51, v51, v63
	v_mul_f32_e32 v102, v102, v110
	v_mul_f32_e32 v102, v96, v102
	v_add_f32_e32 v96, v103, v41
	v_min_f32_e32 v96, 0x40e00000, v96
	v_mul_f32_e32 v103, 0xc01d265f, v96
	v_exp_f32_e32 v103, v103
	v_med3_f32 v51, v51, s63, v230
	v_add_f32_e32 v36, v36, v40
	v_add_f32_e32 v51, 1.0, v51
	v_add_f32_e32 v103, 1.0, v103
	v_rcp_f32_e32 v103, v103
	v_min_f32_e32 v36, 0x40e00000, v36
	v_add_f32_e32 v32, v32, v44
	v_med3_f32 v32, v32, s63, v230
	v_mul_f32_e32 v96, v96, v103
	v_mul_f32_e32 v103, v97, v96
	v_add_f32_e32 v96, v104, v42
	v_min_f32_e32 v96, 0x40e00000, v96
	v_add_f32_e32 v97, v98, v46
	v_mul_f32_e32 v98, 0xc01d265f, v96
	v_exp_f32_e32 v98, v98
	v_med3_f32 v97, v97, s63, v230
	v_add_f32_e32 v97, 1.0, v97
	v_add_f32_e32 v32, 1.0, v32
	v_add_f32_e32 v98, 1.0, v98
	v_rcp_f32_e32 v98, v98
	v_add_f32_e32 v33, v33, v45
	v_med3_f32 v33, v33, s63, v230
	v_add_f32_e32 v33, 1.0, v33
	v_mul_f32_e32 v96, v96, v98
	v_mul_f32_e32 v104, v97, v96
	v_add_f32_e32 v96, v105, v43
	v_min_f32_e32 v96, 0x40e00000, v96
	v_mul_f32_e32 v98, 0xc01d265f, v96
	v_exp_f32_e32 v98, v98
	v_add_f32_e32 v97, v99, v47
	v_med3_f32 v97, v97, s63, v230
	v_add_f32_e32 v97, 1.0, v97
	v_add_f32_e32 v98, 1.0, v98
	v_rcp_f32_e32 v98, v98
	v_add_f32_e32 v28, v28, v56
	v_min_f32_e32 v28, 0x40e00000, v28
	v_add_f32_e32 v24, v24, v60
	v_mul_f32_e32 v96, v96, v98
	v_mul_f32_e32 v99, v97, v96
	v_cvt_pk_bf16_f32 v96, v106, v107
	v_cvt_pk_bf16_f32 v97, v108, v109
	v_cvt_pk_bf16_f32 v98, v102, v103
	v_add_co_u32_e32 v102, vcc, s9, v130
	v_cvt_pk_bf16_f32 v99, v104, v99
	s_mov_b32 s9, 0x18000
	s_nop 0
	v_addc_co_u32_e32 v103, vcc, 0, v131, vcc
	global_store_dwordx4 v[102:103], v[96:99], off
	v_med3_f32 v24, v24, s63, v230
	v_add_f32_e32 v24, 1.0, v24
	v_mul_f32_e32 v96, 0xc01d265f, v92
	v_exp_f32_e32 v96, v96
	v_add_f32_e32 v25, v25, v61
	v_med3_f32 v25, v25, s63, v230
	v_add_f32_e32 v25, 1.0, v25
	v_add_f32_e32 v96, 1.0, v96
	v_rcp_f32_e32 v96, v96
	v_add_f32_e32 v26, v26, v62
	v_med3_f32 v26, v26, s63, v230
	v_add_f32_e32 v26, 1.0, v26
	v_mul_f32_e32 v92, v92, v96
	v_mul_f32_e32 v88, v88, v92
	v_add_f32_e32 v92, v93, v57
	v_min_f32_e32 v92, 0x40e00000, v92
	v_mul_f32_e32 v93, 0xc01d265f, v92
	v_exp_f32_e32 v93, v93
	v_add_f32_e32 v27, v27, v63
	v_med3_f32 v27, v27, s63, v230
	v_add_f32_e32 v20, v20, v40
	v_add_f32_e32 v93, 1.0, v93
	v_rcp_f32_e32 v93, v93
	v_add_f32_e32 v27, 1.0, v27
	v_min_f32_e32 v20, 0x40e00000, v20
	v_add_f32_e32 v16, v16, v44
	v_mul_f32_e32 v92, v92, v93
	v_mul_f32_e32 v89, v89, v92
	v_add_f32_e32 v92, v94, v58
	v_min_f32_e32 v92, 0x40e00000, v92
	v_mul_f32_e32 v93, 0xc01d265f, v92
	v_exp_f32_e32 v93, v93
	v_med3_f32 v16, v16, s63, v230
	v_add_f32_e32 v16, 1.0, v16
	v_add_f32_e32 v17, v17, v45
	v_add_f32_e32 v93, 1.0, v93
	v_rcp_f32_e32 v93, v93
	v_med3_f32 v17, v17, s63, v230
	v_add_f32_e32 v17, 1.0, v17
	v_add_f32_e32 v12, v12, v56
	v_mul_f32_e32 v92, v92, v93
	v_mul_f32_e32 v90, v90, v92
	v_add_f32_e32 v92, v95, v59
	v_min_f32_e32 v92, 0x40e00000, v92
	v_mul_f32_e32 v93, 0xc01d265f, v92
	v_exp_f32_e32 v93, v93
	v_min_f32_e32 v12, 0x40e00000, v12
	v_add_f32_e32 v8, v8, v60
	v_med3_f32 v8, v8, s63, v230
	v_add_f32_e32 v93, 1.0, v93
	v_rcp_f32_e32 v93, v93
	v_add_f32_e32 v8, 1.0, v8
	v_add_f32_e32 v9, v9, v61
	v_med3_f32 v9, v9, s63, v230
	v_mul_f32_e32 v92, v92, v93
	v_mul_f32_e32 v91, v91, v92
	v_mul_f32_e32 v92, 0xc01d265f, v84
	v_exp_f32_e32 v92, v92
	v_add_f32_e32 v9, 1.0, v9
	v_add_f32_e32 v10, v10, v62
	v_med3_f32 v10, v10, s63, v230
	v_add_f32_e32 v92, 1.0, v92
	v_rcp_f32_e32 v92, v92
	v_add_f32_e32 v10, 1.0, v10
	v_add_f32_e32 v11, v11, v63
	v_med3_f32 v11, v11, s63, v230
	v_mul_f32_e32 v84, v84, v92
	v_mul_f32_e32 v84, v80, v84
	v_add_f32_e32 v80, v85, v41
	v_min_f32_e32 v80, 0x40e00000, v80
	v_mul_f32_e32 v85, 0xc01d265f, v80
	v_exp_f32_e32 v85, v85
	v_add_f32_e32 v4, v4, v40
	v_add_f32_e32 v11, 1.0, v11
	v_min_f32_e32 v4, 0x40e00000, v4
	v_add_f32_e32 v85, 1.0, v85
	v_rcp_f32_e32 v85, v85
	v_add_f32_e32 v0, v0, v44
	v_med3_f32 v0, v0, s63, v230
	v_add_f32_e32 v0, 1.0, v0
	v_mul_f32_e32 v80, v80, v85
	v_mul_f32_e32 v85, v81, v80
	v_add_f32_e32 v80, v86, v42
	v_min_f32_e32 v80, 0x40e00000, v80
	v_add_f32_e32 v81, v82, v46
	v_mul_f32_e32 v82, 0xc01d265f, v80
	v_exp_f32_e32 v82, v82
	v_med3_f32 v81, v81, s63, v230
	v_add_f32_e32 v81, 1.0, v81
	v_add_f32_e32 v1, v1, v45
	v_add_f32_e32 v82, 1.0, v82
	v_rcp_f32_e32 v82, v82
	v_med3_f32 v1, v1, s63, v230
	v_add_f32_e32 v1, 1.0, v1
	s_mov_b64 s[28:29], -1
	v_mul_f32_e32 v80, v80, v82
	v_mul_f32_e32 v86, v81, v80
	v_add_f32_e32 v80, v87, v43
	v_min_f32_e32 v80, 0x40e00000, v80
	v_mul_f32_e32 v82, 0xc01d265f, v80
	v_exp_f32_e32 v82, v82
	v_add_f32_e32 v81, v83, v47
	v_med3_f32 v81, v81, s63, v230
	v_add_f32_e32 v81, 1.0, v81
	v_add_f32_e32 v82, 1.0, v82
	v_rcp_f32_e32 v82, v82
	s_nop 0
	v_mul_f32_e32 v80, v80, v82
	v_mul_f32_e32 v83, v81, v80
	v_cvt_pk_bf16_f32 v80, v88, v89
	v_cvt_pk_bf16_f32 v81, v90, v91
	v_cvt_pk_bf16_f32 v82, v84, v85
	v_add_co_u32_e32 v84, vcc, s9, v130
	v_cvt_pk_bf16_f32 v83, v86, v83
	s_mov_b32 s9, 0x40000
	s_nop 0
	v_addc_co_u32_e32 v85, vcc, 0, v131, vcc
	global_store_dwordx4 v[84:85], v[80:83], off
	s_nop 1
	v_mul_f32_e32 v80, 0xc01d265f, v76
	v_exp_f32_e32 v80, v80
	s_nop 0
	v_add_f32_e32 v80, 1.0, v80
	v_rcp_f32_e32 v80, v80
	s_nop 0
	v_mul_f32_e32 v76, v76, v80
	v_mul_f32_e32 v72, v72, v76
	v_add_f32_e32 v76, v77, v57
	v_min_f32_e32 v76, 0x40e00000, v76
	v_mul_f32_e32 v77, 0xc01d265f, v76
	v_exp_f32_e32 v77, v77
	s_nop 0
	v_add_f32_e32 v77, 1.0, v77
	v_rcp_f32_e32 v77, v77
	s_nop 0
	v_mul_f32_e32 v76, v76, v77
	v_mul_f32_e32 v73, v73, v76
	v_add_f32_e32 v76, v78, v58
	v_min_f32_e32 v76, 0x40e00000, v76
	v_mul_f32_e32 v77, 0xc01d265f, v76
	v_exp_f32_e32 v77, v77
	s_nop 0
	v_add_f32_e32 v77, 1.0, v77
	v_rcp_f32_e32 v77, v77
	s_nop 0
	v_mul_f32_e32 v76, v76, v77
	v_mul_f32_e32 v74, v74, v76
	v_add_f32_e32 v76, v79, v59
	v_min_f32_e32 v76, 0x40e00000, v76
	v_mul_f32_e32 v77, 0xc01d265f, v76
	v_exp_f32_e32 v77, v77
	s_nop 0
	v_add_f32_e32 v77, 1.0, v77
	v_rcp_f32_e32 v77, v77
	s_nop 0
	v_mul_f32_e32 v76, v76, v77
	v_mul_f32_e32 v75, v75, v76
	v_mul_f32_e32 v76, 0xc01d265f, v68
	v_exp_f32_e32 v76, v76
	s_nop 0
	v_add_f32_e32 v76, 1.0, v76
	v_rcp_f32_e32 v76, v76
	s_nop 0
	v_mul_f32_e32 v68, v68, v76
	v_mul_f32_e32 v68, v64, v68
	v_add_f32_e32 v64, v69, v41
	v_min_f32_e32 v64, 0x40e00000, v64
	v_mul_f32_e32 v69, 0xc01d265f, v64
	v_exp_f32_e32 v69, v69
	s_nop 0
	v_add_f32_e32 v69, 1.0, v69
	v_rcp_f32_e32 v69, v69
	s_nop 0
	v_mul_f32_e32 v64, v64, v69
	v_mul_f32_e32 v69, v65, v64
	v_add_f32_e32 v64, v70, v42
	v_min_f32_e32 v64, 0x40e00000, v64
	v_add_f32_e32 v65, v66, v46
	v_mul_f32_e32 v66, 0xc01d265f, v64
	v_exp_f32_e32 v66, v66
	v_med3_f32 v65, v65, s63, v230
	v_add_f32_e32 v65, 1.0, v65
	v_add_f32_e32 v66, 1.0, v66
	v_rcp_f32_e32 v66, v66
	s_nop 0
	v_mul_f32_e32 v64, v64, v66
	v_mul_f32_e32 v70, v65, v64
	v_add_f32_e32 v64, v71, v43
	v_min_f32_e32 v64, 0x40e00000, v64
	v_mul_f32_e32 v66, 0xc01d265f, v64
	v_exp_f32_e32 v66, v66
	v_add_f32_e32 v65, v67, v47
	v_med3_f32 v65, v65, s63, v230
	v_add_f32_e32 v65, 1.0, v65
	v_add_f32_e32 v66, 1.0, v66
	v_rcp_f32_e32 v66, v66
	s_nop 0
	v_mul_f32_e32 v64, v64, v66
	v_mul_f32_e32 v67, v65, v64
	v_cvt_pk_bf16_f32 v64, v72, v73
	v_cvt_pk_bf16_f32 v65, v74, v75
	v_cvt_pk_bf16_f32 v66, v68, v69
	v_add_co_u32_e32 v68, vcc, s9, v130
	v_cvt_pk_bf16_f32 v67, v70, v67
	s_mov_b32 s9, 0x48000
	s_nop 0
	v_addc_co_u32_e32 v69, vcc, 0, v131, vcc
	global_store_dwordx4 v[68:69], v[64:67], off
	s_nop 1
	v_mul_f32_e32 v64, 0xc01d265f, v52
	v_exp_f32_e32 v64, v64
	s_nop 0
	v_add_f32_e32 v64, 1.0, v64
	v_rcp_f32_e32 v64, v64
	s_nop 0
	v_mul_f32_e32 v52, v52, v64
	v_mul_f32_e32 v48, v48, v52
	v_add_f32_e32 v52, v53, v57
	v_min_f32_e32 v52, 0x40e00000, v52
	v_mul_f32_e32 v53, 0xc01d265f, v52
	v_exp_f32_e32 v53, v53
	s_nop 0
	v_add_f32_e32 v53, 1.0, v53
	v_rcp_f32_e32 v53, v53
	s_nop 0
	v_mul_f32_e32 v52, v52, v53
	v_mul_f32_e32 v49, v49, v52
	v_add_f32_e32 v52, v54, v58
	v_min_f32_e32 v52, 0x40e00000, v52
	v_mul_f32_e32 v53, 0xc01d265f, v52
	v_exp_f32_e32 v53, v53
	s_nop 0
	v_add_f32_e32 v53, 1.0, v53
	v_rcp_f32_e32 v53, v53
	s_nop 0
	v_mul_f32_e32 v52, v52, v53
	v_mul_f32_e32 v50, v50, v52
	v_add_f32_e32 v52, v55, v59
	v_min_f32_e32 v52, 0x40e00000, v52
	v_mul_f32_e32 v53, 0xc01d265f, v52
	v_exp_f32_e32 v53, v53
	s_nop 0
	v_add_f32_e32 v53, 1.0, v53
	v_rcp_f32_e32 v53, v53
	s_nop 0
	v_mul_f32_e32 v52, v52, v53
	v_mul_f32_e32 v51, v51, v52
	v_mul_f32_e32 v52, 0xc01d265f, v36
	v_exp_f32_e32 v52, v52
	s_nop 0
	v_add_f32_e32 v52, 1.0, v52
	v_rcp_f32_e32 v52, v52
	s_nop 0
	v_mul_f32_e32 v36, v36, v52
	v_mul_f32_e32 v36, v32, v36
	v_add_f32_e32 v32, v37, v41
	v_min_f32_e32 v32, 0x40e00000, v32
	v_mul_f32_e32 v37, 0xc01d265f, v32
	v_exp_f32_e32 v37, v37
	s_nop 0
	v_add_f32_e32 v37, 1.0, v37
	v_rcp_f32_e32 v37, v37
	s_nop 0
	v_mul_f32_e32 v32, v32, v37
	v_mul_f32_e32 v37, v33, v32
	v_add_f32_e32 v32, v38, v42
	v_min_f32_e32 v32, 0x40e00000, v32
	v_add_f32_e32 v33, v34, v46
	v_mul_f32_e32 v34, 0xc01d265f, v32
	v_exp_f32_e32 v34, v34
	v_med3_f32 v33, v33, s63, v230
	v_add_f32_e32 v33, 1.0, v33
	v_add_f32_e32 v34, 1.0, v34
	v_rcp_f32_e32 v34, v34
	s_nop 0
	v_mul_f32_e32 v32, v32, v34
	v_mul_f32_e32 v38, v33, v32
	v_add_f32_e32 v32, v39, v43
	v_min_f32_e32 v32, 0x40e00000, v32
	v_mul_f32_e32 v34, 0xc01d265f, v32
	v_exp_f32_e32 v34, v34
	v_add_f32_e32 v33, v35, v47
	v_med3_f32 v33, v33, s63, v230
	v_add_f32_e32 v33, 1.0, v33
	v_add_f32_e32 v34, 1.0, v34
	v_rcp_f32_e32 v34, v34
	s_nop 0
	v_mul_f32_e32 v32, v32, v34
	v_mul_f32_e32 v35, v33, v32
	v_cvt_pk_bf16_f32 v32, v48, v49
	v_cvt_pk_bf16_f32 v33, v50, v51
	v_cvt_pk_bf16_f32 v34, v36, v37
	v_add_co_u32_e32 v36, vcc, s9, v130
	v_cvt_pk_bf16_f32 v35, v38, v35
	s_mov_b32 s9, 0x50000
	s_nop 0
	v_addc_co_u32_e32 v37, vcc, 0, v131, vcc
	global_store_dwordx4 v[36:37], v[32:35], off
	s_nop 1
	v_mul_f32_e32 v32, 0xc01d265f, v28
	v_exp_f32_e32 v32, v32
	s_nop 0
	v_add_f32_e32 v32, 1.0, v32
	v_rcp_f32_e32 v32, v32
	s_nop 0
	v_mul_f32_e32 v28, v28, v32
	v_mul_f32_e32 v24, v24, v28
	v_add_f32_e32 v28, v29, v57
	v_min_f32_e32 v28, 0x40e00000, v28
	v_mul_f32_e32 v29, 0xc01d265f, v28
	v_exp_f32_e32 v29, v29
	s_nop 0
	v_add_f32_e32 v29, 1.0, v29
	v_rcp_f32_e32 v29, v29
	s_nop 0
	v_mul_f32_e32 v28, v28, v29
	v_mul_f32_e32 v25, v25, v28
	v_add_f32_e32 v28, v30, v58
	v_min_f32_e32 v28, 0x40e00000, v28
	v_mul_f32_e32 v29, 0xc01d265f, v28
	v_exp_f32_e32 v29, v29
	s_nop 0
	v_add_f32_e32 v29, 1.0, v29
	v_rcp_f32_e32 v29, v29
	s_nop 0
	v_mul_f32_e32 v28, v28, v29
	v_mul_f32_e32 v26, v26, v28
	v_add_f32_e32 v28, v31, v59
	v_min_f32_e32 v28, 0x40e00000, v28
	v_mul_f32_e32 v29, 0xc01d265f, v28
	v_exp_f32_e32 v29, v29
	s_nop 0
	v_add_f32_e32 v29, 1.0, v29
	v_rcp_f32_e32 v29, v29
	s_nop 0
	v_mul_f32_e32 v28, v28, v29
	v_mul_f32_e32 v27, v27, v28
	v_mul_f32_e32 v28, 0xc01d265f, v20
	v_exp_f32_e32 v28, v28
	s_nop 0
	v_add_f32_e32 v28, 1.0, v28
	v_rcp_f32_e32 v28, v28
	s_nop 0
	v_mul_f32_e32 v20, v20, v28
	v_mul_f32_e32 v20, v16, v20
	v_add_f32_e32 v16, v21, v41
	v_min_f32_e32 v16, 0x40e00000, v16
	v_mul_f32_e32 v21, 0xc01d265f, v16
	v_exp_f32_e32 v21, v21
	s_nop 0
	v_add_f32_e32 v21, 1.0, v21
	v_rcp_f32_e32 v21, v21
	s_nop 0
	v_mul_f32_e32 v16, v16, v21
	v_mul_f32_e32 v21, v17, v16
	v_add_f32_e32 v16, v22, v42
	v_min_f32_e32 v16, 0x40e00000, v16
	v_add_f32_e32 v17, v18, v46
	v_mul_f32_e32 v18, 0xc01d265f, v16
	v_exp_f32_e32 v18, v18
	v_med3_f32 v17, v17, s63, v230
	v_add_f32_e32 v17, 1.0, v17
	v_add_f32_e32 v18, 1.0, v18
	v_rcp_f32_e32 v18, v18
	s_nop 0
	v_mul_f32_e32 v16, v16, v18
	v_mul_f32_e32 v22, v17, v16
	v_add_f32_e32 v16, v23, v43
	v_min_f32_e32 v16, 0x40e00000, v16
	v_mul_f32_e32 v18, 0xc01d265f, v16
	v_exp_f32_e32 v18, v18
	v_add_f32_e32 v17, v19, v47
	v_med3_f32 v17, v17, s63, v230
	v_add_f32_e32 v17, 1.0, v17
	v_add_f32_e32 v18, 1.0, v18
	v_rcp_f32_e32 v18, v18
	s_nop 0
	v_mul_f32_e32 v16, v16, v18
	v_mul_f32_e32 v19, v17, v16
	v_cvt_pk_bf16_f32 v16, v24, v25
	v_cvt_pk_bf16_f32 v17, v26, v27
	v_cvt_pk_bf16_f32 v18, v20, v21
	v_add_co_u32_e32 v20, vcc, s9, v130
	v_cvt_pk_bf16_f32 v19, v22, v19
	s_nop 1
	v_addc_co_u32_e32 v21, vcc, 0, v131, vcc
	global_store_dwordx4 v[20:21], v[16:19], off
	s_nop 1
	v_mul_f32_e32 v16, 0xc01d265f, v12
	v_exp_f32_e32 v16, v16
	s_nop 0
	v_add_f32_e32 v16, 1.0, v16
	v_rcp_f32_e32 v16, v16
	s_nop 0
	v_mul_f32_e32 v12, v12, v16
	v_mul_f32_e32 v8, v8, v12
	v_add_f32_e32 v12, v13, v57
	v_min_f32_e32 v12, 0x40e00000, v12
	v_mul_f32_e32 v13, 0xc01d265f, v12
	v_exp_f32_e32 v13, v13
	s_nop 0
	v_add_f32_e32 v13, 1.0, v13
	v_rcp_f32_e32 v13, v13
	s_nop 0
	v_mul_f32_e32 v12, v12, v13
	v_mul_f32_e32 v9, v9, v12
	v_add_f32_e32 v12, v14, v58
	v_min_f32_e32 v12, 0x40e00000, v12
	v_mul_f32_e32 v13, 0xc01d265f, v12
	v_exp_f32_e32 v13, v13
	s_nop 0
	v_add_f32_e32 v13, 1.0, v13
	v_rcp_f32_e32 v13, v13
	s_nop 0
	v_mul_f32_e32 v12, v12, v13
	v_mul_f32_e32 v10, v10, v12
	v_add_f32_e32 v12, v15, v59
	v_min_f32_e32 v12, 0x40e00000, v12
	v_mul_f32_e32 v13, 0xc01d265f, v12
	v_exp_f32_e32 v13, v13
	s_nop 0
	v_add_f32_e32 v13, 1.0, v13
	v_rcp_f32_e32 v13, v13
	s_nop 0
	v_mul_f32_e32 v12, v12, v13
	v_mul_f32_e32 v11, v11, v12
	v_mul_f32_e32 v12, 0xc01d265f, v4
	v_exp_f32_e32 v12, v12
	s_nop 0
	v_add_f32_e32 v12, 1.0, v12
	v_rcp_f32_e32 v12, v12
	s_nop 0
	v_mul_f32_e32 v4, v4, v12
	v_mul_f32_e32 v4, v0, v4
	v_add_f32_e32 v0, v5, v41
	v_min_f32_e32 v0, 0x40e00000, v0
	v_mul_f32_e32 v5, 0xc01d265f, v0
	v_exp_f32_e32 v5, v5
	s_nop 0
	v_add_f32_e32 v5, 1.0, v5
	v_rcp_f32_e32 v5, v5
	s_nop 0
	v_mul_f32_e32 v0, v0, v5
	v_mul_f32_e32 v5, v1, v0
	v_add_f32_e32 v0, v6, v42
	v_min_f32_e32 v0, 0x40e00000, v0
	v_add_f32_e32 v1, v2, v46
	v_mul_f32_e32 v2, 0xc01d265f, v0
	v_exp_f32_e32 v2, v2
	v_med3_f32 v1, v1, s63, v230
	v_add_f32_e32 v1, 1.0, v1
	v_add_f32_e32 v2, 1.0, v2
	v_rcp_f32_e32 v2, v2
	s_nop 0
	v_mul_f32_e32 v0, v0, v2
	v_mul_f32_e32 v6, v1, v0
	v_add_f32_e32 v0, v7, v43
	v_min_f32_e32 v0, 0x40e00000, v0
	v_mul_f32_e32 v2, 0xc01d265f, v0
	v_exp_f32_e32 v2, v2
	v_add_f32_e32 v1, v3, v47
	v_med3_f32 v1, v1, s63, v230
	v_add_f32_e32 v1, 1.0, v1
	v_add_f32_e32 v2, 1.0, v2
	v_rcp_f32_e32 v2, v2
	s_nop 0
	v_mul_f32_e32 v0, v0, v2
	v_mul_f32_e32 v3, v1, v0
	v_cvt_pk_bf16_f32 v0, v8, v9
	v_cvt_pk_bf16_f32 v1, v10, v11
	v_cvt_pk_bf16_f32 v2, v4, v5
	v_add_co_u32_e32 v4, vcc, 0x58000, v130
	v_cvt_pk_bf16_f32 v3, v6, v3
	s_nop 1
	v_addc_co_u32_e32 v5, vcc, 0, v131, vcc
	s_andn2_b64 vcc, exec, s[24:25]
	global_store_dwordx4 v[4:5], v[0:3], off
	s_cbranch_vccnz .LBB0_1509
	s_andn2_b64 vcc, exec, s[12:13]
	s_cbranch_vccnz .LBB0_1508
	s_barrier
	s_branch .LBB0_1508
